# compiled P10 with 4 consecutive rows per wave (induction constants only); on top of P2 consecutive rows + barrier early invalidate
# baseline (speedup 1.0000x reference)
; __device__ __forceinline__ void combine_row(int m, int lane, const float* __restrict__ h1, const bf16* __restrict__ y, const unsigned* __restrict__ cnt, const int* __restrict__ tok_e, const int* __restrict__ tok_p, ...
;     size_t yrow[4]; float gk[4];
; #pragma unroll
;     for (int k = 0; k < 4; ++k) {
;         const int e = tok_e[m * 4 + k]; const int off = (int)cnt[e];
;         yrow[k] = (size_t)(off + tok_p[m * 4 + k]) * D; gk[k] = gate[m * 4 + k];
;     }
;     f32x4 v[8]; float ss = 0.f;
; #pragma unroll
;     for (int j = 0; j < 8; ++j) {
;         const int idx = j * 256 + lane * 4;
;         f32x4 a = *(const f32x4*)(h1 + (size_t)m * D + idx);
; #pragma unroll
;         for (int k = 0; k < 4; ++k) { const u32x2 w = *(const u32x2*)(y + yrow[k] + idx);
; __device__ __forceinline__ void phase10() { const Ctx c = make_ctx(); PHASE_PTRS; for (int m = c.gw; m < M; m += c.NGW) combine_row(m, c.lane, h1, y, (const unsigned*)(ws + WS_CTL) + CW_OFFT, tok_e, tok_p, gate, INP(19), ka->out); }
.LBB0_1576:
	v_readlane_b32 s0, v252, 0
	v_readlane_b32 s1, v252, 1
	s_cmp_lt_i32 s0, 11
	s_cselect_b64 s[0:1], -1, 0
	s_and_b64 s[0:1], s[0:1], s[4:5]
	s_andn2_b64 vcc, exec, s[0:1]
	s_cbranch_vccnz .LBB0_1580
	s_nop 0
	v_readfirstlane_b32 s0, v0
	s_ashr_i32 s16, s0, 6
	s_lshl_b32 s0, s2, 3
	s_add_i32 s8, s16, s0
	s_lshl_b32 s0, s3, 3
	s_mov_b32 s99, 1
.Lp10c_rpw:
	s_mul_i32 s1, s99, s0
	s_cmpk_lt_u32 s1, 0x2000
	s_cbranch_scc0 .Lp10c_done
	s_add_i32 s99, s99, 1
	s_branch .Lp10c_rpw
.Lp10c_done:
	s_mul_i32 s8, s8, s99
	s_add_i32 s99, s8, s99
	s_min_i32 s99, s99, 0x2000
	s_cmpk_gt_i32 s8, 0x1fff
	s_cbranch_scc1 .LBB0_1580
	s_load_dwordx4 s[4:7], s[94:95], 0x98
	s_load_dwordx2 s[14:15], s[94:95], 0xa8
	v_lshlrev_b32_e32 v1, 2, v0
	v_and_b32_e32 v1, 0xfc, v1
	s_waitcnt vmcnt(0)
	v_lshlrev_b32_e32 v18, 2, v1
	v_or_b32_e32 v34, 0x400, v1
	v_or_b32_e32 v36, 0x500, v1
	v_or_b32_e32 v38, 0x600, v1
	s_waitcnt lgkmcnt(0)
	global_load_dwordx4 v[2:5], v18, s[4:5]
	global_load_dwordx4 v[6:9], v18, s[4:5] offset:1024
	global_load_dwordx4 v[10:13], v18, s[4:5] offset:2048
	global_load_dwordx4 v[14:17], v18, s[4:5] offset:3072
	v_or_b32_e32 v40, 0x700, v1
	v_lshlrev_b32_e32 v26, 2, v34
	v_lshlrev_b32_e32 v27, 2, v36
	v_lshlrev_b32_e32 v35, 2, v38
	global_load_dwordx4 v[18:21], v26, s[4:5]
	global_load_dwordx4 v[22:25], v27, s[4:5]
	v_lshlrev_b32_e32 v37, 2, v40
	global_load_dwordx4 v[26:29], v35, s[4:5]
	global_load_dwordx4 v[30:33], v37, s[4:5]
	v_lshlrev_b32_e32 v62, 1, v1
	v_or_b32_e32 v42, 0x100, v1
	v_or_b32_e32 v44, 0x200, v1
	v_or_b32_e32 v46, 0x300, v1
	v_mbcnt_lo_u32_b32 v1, -1, 0
	v_mbcnt_hi_u32_b32 v1, -1, v1
	v_and_b32_e32 v35, 64, v1
	v_add_u32_e32 v35, 64, v35
	v_xor_b32_e32 v37, 1, v1
	s_mov_b32 s0, 1
	v_cmp_lt_i32_e32 vcc, v37, v35
	s_add_u32 s18, s14, 0x47e00000
	s_addc_u32 s19, s15, 0
	v_cndmask_b32_e32 v37, v1, v37, vcc
	v_lshlrev_b32_e32 v74, 2, v37
	v_xor_b32_e32 v37, 2, v1
	s_add_u32 s20, s14, 0x47f00000
	v_cmp_lt_i32_e32 vcc, v37, v35
	s_addc_u32 s21, s15, 0
	s_add_u32 s22, s14, 0x48000000
	v_cndmask_b32_e32 v37, v1, v37, vcc
	v_lshlrev_b32_e32 v75, 2, v37
	v_xor_b32_e32 v37, 4, v1
	s_addc_u32 s23, s15, 0
	v_cmp_lt_i32_e32 vcc, v37, v35
	s_add_u32 s4, s14, 0x52400000
	s_addc_u32 s5, s15, 0
	v_cndmask_b32_e32 v37, v1, v37, vcc
	v_lshlrev_b32_e32 v76, 2, v37
	v_xor_b32_e32 v37, 8, v1
	s_add_u32 s10, s14, 0x1700
	v_cmp_lt_i32_e32 vcc, v37, v35
	s_addc_u32 s11, s15, 0
	s_ashr_i32 s9, s8, 31
	v_cndmask_b32_e32 v37, v1, v37, vcc
	v_lshlrev_b32_e32 v77, 2, v37
	v_xor_b32_e32 v37, 16, v1
	s_lshl_b64 s[24:25], s[8:9], 13
	v_cmp_lt_i32_e32 vcc, v37, v35
	s_add_u32 s6, s6, s24
	s_addc_u32 s7, s7, s25
	v_cndmask_b32_e32 v37, v1, v37, vcc
	s_ashr_i32 s1, s0, 31
	v_lshlrev_b32_e32 v78, 2, v37
	v_xor_b32_e32 v37, 32, v1
	s_lshl_b64 s[12:13], s[0:1], 13
	s_lshl_b32 s2, s8, 2
	s_nop 0
	v_cmp_lt_i32_e32 vcc, v37, v35
	s_nop 0
	s_mov_b32 s1, 4
	v_mov_b32_e32 v63, 0
	v_cndmask_b32_e32 v1, v1, v37, vcc
	v_and_b32_e32 v0, 63, v0
	s_add_u32 s14, s14, s24
	v_lshl_add_u64 v[64:65], s[4:5], 0, v[62:63]
	v_lshlrev_b32_e32 v79, 2, v1
	v_lshlrev_b32_e32 v62, 4, v0
	s_addc_u32 s15, s15, s25
	s_mov_b32 s9, 0x41e00000
	v_lshlrev_b32_e32 v80, 1, v42
	v_lshlrev_b32_e32 v81, 1, v44
	v_lshlrev_b32_e32 v82, 1, v46
	s_mov_b32 s24, 0x41e01000
	v_lshlrev_b32_e32 v83, 1, v34
	v_lshlrev_b32_e32 v84, 1, v36
	v_lshlrev_b32_e32 v85, 1, v38
	v_lshlrev_b32_e32 v86, 1, v40
	v_mov_b32_e32 v87, 0x358637bd
	s_mov_b32 s25, 0x800000
	s_movk_i32 s26, 0x1000
.LBB0_1579:
	s_ashr_i32 s3, s2, 31
	v_lshl_add_u64 v[34:35], s[14:15], 0, v[62:63]
	s_lshl_b64 s[16:17], s[2:3], 2
	v_add_co_u32_e32 v68, vcc, s9, v34
	s_add_u32 s28, s18, s16
	s_nop 0
	v_addc_co_u32_e32 v69, vcc, 0, v35, vcc
	v_add_co_u32_e32 v70, vcc, s24, v34
	s_addc_u32 s29, s19, s17
	s_nop 0
	v_addc_co_u32_e32 v71, vcc, 0, v35, vcc
	global_load_dwordx4 v[58:61], v[68:69], off offset:1024
	global_load_dwordx4 v[54:57], v[68:69], off offset:2048
	global_load_dwordx4 v[46:49], v[68:69], off offset:3072
	global_load_dwordx4 v[88:91], v[70:71], off offset:-4096
	global_load_dwordx4 v[50:53], v[70:71], off
	global_load_dwordx4 v[42:45], v[70:71], off offset:1024
	global_load_dwordx4 v[38:41], v[70:71], off offset:2048
	global_load_dwordx4 v[34:37], v[70:71], off offset:3072
	global_load_dwordx4 v[92:95], v63, s[28:29]
	s_add_u32 s28, s20, s16
	s_addc_u32 s29, s21, s17
	s_add_u32 s16, s22, s16
	s_addc_u32 s17, s23, s17
	global_load_dword v69, v63, s[28:29]
	global_load_dword v70, v63, s[16:17]
	s_add_i32 s28, s2, 1
	s_ashr_i32 s29, s28, 31
	s_lshl_b64 s[16:17], s[28:29], 2
	s_add_u32 s28, s20, s16
	s_addc_u32 s29, s21, s17
	s_add_u32 s16, s22, s16
	s_addc_u32 s17, s23, s17
	global_load_dwordx3 v[96:98], v63, s[28:29]
	global_load_dword v68, v63, s[16:17]
	s_add_i32 s28, s2, 2
	s_ashr_i32 s29, s28, 31
	s_lshl_b64 s[16:17], s[28:29], 2
	s_add_u32 s16, s22, s16
	s_addc_u32 s17, s23, s17
	global_load_dwordx2 v[72:73], v63, s[16:17]
	v_lshl_add_u64 v[0:1], s[6:7], 0, v[62:63]
	v_add_co_u32_e32 v66, vcc, s26, v0
	s_add_i32 s8, s8, s0
	s_nop 0
	v_addc_co_u32_e32 v67, vcc, 0, v1, vcc
	s_add_u32 s6, s6, s12
	s_addc_u32 s7, s7, s13
	s_add_i32 s2, s2, s1
	s_add_u32 s14, s14, s12
	s_addc_u32 s15, s15, s13
	s_cmp_lt_i32 s8, s99
	s_waitcnt vmcnt(5)
	v_ashrrev_i32_e32 v101, 31, v92
	v_mov_b32_e32 v100, v92
	v_ashrrev_i32_e32 v103, 31, v93
	v_mov_b32_e32 v102, v93
	v_ashrrev_i32_e32 v93, 31, v94
	v_mov_b32_e32 v92, v94
	v_ashrrev_i32_e32 v105, 31, v95
	v_mov_b32_e32 v104, v95
	v_lshlrev_b64 v[94:95], 2, v[100:101]
	v_lshlrev_b64 v[100:101], 2, v[102:103]
	v_lshlrev_b64 v[92:93], 2, v[92:93]
	v_lshlrev_b64 v[102:103], 2, v[104:105]
	v_lshl_add_u64 v[94:95], s[10:11], 0, v[94:95]
	v_lshl_add_u64 v[100:101], s[10:11], 0, v[100:101]
	v_lshl_add_u64 v[92:93], s[10:11], 0, v[92:93]
	v_lshl_add_u64 v[102:103], s[10:11], 0, v[102:103]
	global_load_dword v71, v[94:95], off
	global_load_dword v99, v[100:101], off
	global_load_dword v104, v[92:93], off
	global_load_dword v105, v[102:103], off
	s_waitcnt vmcnt(3)
; __device__ __forceinline__ void combine_row(int m, int lane, const float* __restrict__ h1, const bf16* __restrict__ y, const unsigned* __restrict__ cnt, const int* __restrict__ tok_e, const int* __restrict__ tok_p, ...
;     ...
;     for (int k = 0; k < 4; ++k) {
;         const int e = tok_e[m * 4 + k]; const int off = (int)cnt[e];
;         yrow[k] = (size_t)(off + tok_p[m * 4 + k]) * D; gk[k] = gate[m * 4 + k];
;     }
;     f32x4 v[8]; float ss = 0.f;
; #pragma unroll
;     for (int j = 0; j < 8; ++j) {
;         const int idx = j * 256 + lane * 4;
;         f32x4 a = *(const f32x4*)(h1 + (size_t)m * D + idx);
; #pragma unroll
;         for (int k = 0; k < 4; ++k) { const u32x2 w = *(const u32x2*)(y + yrow[k] + idx);
;             a.x += gk[k] * __uint_as_float(w.x << 16); a.y += gk[k] * __uint_as_float(w.x & 0xffff0000u); a.z += gk[k] * __uint_as_float(w.y << 16); a.w += gk[k] * __uint_as_float(w.y & 0xffff0000u); }
	v_add_u32_e32 v92, v69, v71
	s_waitcnt vmcnt(2)
	v_add_u32_e32 v94, v96, v99
	s_waitcnt vmcnt(1)
	v_add_u32_e32 v96, v97, v104
	s_waitcnt vmcnt(0)
	v_add_u32_e32 v98, v98, v105
	v_ashrrev_i32_e32 v93, 31, v92
	v_ashrrev_i32_e32 v95, 31, v94
	v_ashrrev_i32_e32 v97, 31, v96
	v_ashrrev_i32_e32 v99, 31, v98
	v_lshlrev_b64 v[92:93], 12, v[92:93]
	v_lshlrev_b64 v[94:95], 12, v[94:95]
	v_lshlrev_b64 v[96:97], 12, v[96:97]
	v_lshlrev_b64 v[98:99], 12, v[98:99]
	v_lshl_add_u64 v[100:101], v[64:65], 0, v[92:93]
	v_lshl_add_u64 v[92:93], s[4:5], 0, v[92:93]
	v_lshl_add_u64 v[102:103], v[64:65], 0, v[94:95]
	v_lshl_add_u64 v[104:105], v[64:65], 0, v[96:97]
	v_lshl_add_u64 v[106:107], v[64:65], 0, v[98:99]
	v_lshl_add_u64 v[94:95], s[4:5], 0, v[94:95]
	v_lshl_add_u64 v[96:97], s[4:5], 0, v[96:97]
	v_lshl_add_u64 v[98:99], s[4:5], 0, v[98:99]
	global_load_dwordx2 v[108:109], v[100:101], off
	global_load_dwordx2 v[110:111], v[102:103], off
	global_load_dwordx2 v[112:113], v[104:105], off
	global_load_dwordx2 v[114:115], v[106:107], off
	v_readfirstlane_b32 s16, v92
	v_readfirstlane_b32 s17, v93
	v_readfirstlane_b32 s28, v94
	v_readfirstlane_b32 s29, v95
	v_readfirstlane_b32 s30, v96
	v_readfirstlane_b32 s31, v97
	v_readfirstlane_b32 s34, v98
	v_readfirstlane_b32 s35, v99
	global_load_dwordx2 v[92:93], v80, s[16:17]
	global_load_dwordx2 v[94:95], v80, s[28:29]
	s_nop 0
	global_load_dwordx2 v[96:97], v80, s[30:31]
	s_nop 0
	global_load_dwordx2 v[98:99], v80, s[34:35]
	global_load_dwordx2 v[100:101], v81, s[16:17]
	global_load_dwordx2 v[102:103], v81, s[28:29]
	global_load_dwordx2 v[104:105], v81, s[30:31]
	global_load_dwordx2 v[106:107], v81, s[34:35]
	global_load_dwordx2 v[116:117], v82, s[16:17]
	global_load_dwordx2 v[118:119], v82, s[28:29]
	global_load_dwordx2 v[120:121], v82, s[30:31]
	global_load_dwordx2 v[122:123], v82, s[34:35]
	global_load_dwordx2 v[124:125], v83, s[16:17]
	global_load_dwordx2 v[126:127], v83, s[28:29]
	global_load_dwordx2 v[128:129], v83, s[30:31]
	global_load_dwordx2 v[130:131], v83, s[34:35]
	global_load_dwordx2 v[132:133], v84, s[16:17]
	global_load_dwordx2 v[134:135], v84, s[28:29]
	global_load_dwordx2 v[136:137], v84, s[30:31]
	global_load_dwordx2 v[138:139], v84, s[34:35]
	global_load_dwordx2 v[140:141], v85, s[16:17]
	global_load_dwordx2 v[142:143], v85, s[28:29]
	global_load_dwordx2 v[144:145], v85, s[30:31]
	global_load_dwordx2 v[146:147], v85, s[34:35]
	global_load_dwordx2 v[148:149], v86, s[16:17]
	global_load_dwordx2 v[150:151], v86, s[28:29]
	global_load_dwordx2 v[152:153], v86, s[30:31]
	global_load_dwordx2 v[154:155], v86, s[34:35]
	s_waitcnt vmcnt(25)
	v_lshlrev_b32_e32 v164, 16, v96
	v_and_b32_e32 v165, 0xffff0000, v96
	s_waitcnt vmcnt(23)
	v_lshlrev_b32_e32 v168, 16, v100
	v_and_b32_e32 v169, 0xffff0000, v100
	v_lshlrev_b32_e32 v100, 16, v101
	v_and_b32_e32 v101, 0xffff0000, v101
	s_waitcnt vmcnt(19)
	v_lshlrev_b32_e32 v176, 16, v116
	v_and_b32_e32 v177, 0xffff0000, v116
	v_lshlrev_b32_e32 v116, 16, v117
	v_and_b32_e32 v117, 0xffff0000, v117
	s_waitcnt vmcnt(15)
	v_lshlrev_b32_e32 v184, 16, v124
	v_and_b32_e32 v185, 0xffff0000, v124
	s_waitcnt vmcnt(14)
	v_lshlrev_b32_e32 v186, 16, v126
	v_lshlrev_b32_e32 v156, 16, v108
	v_and_b32_e32 v157, 0xffff0000, v108
	v_lshlrev_b32_e32 v108, 16, v109
	v_and_b32_e32 v109, 0xffff0000, v109
	v_pk_fma_f32 v[90:91], v[70:71], v[108:109], v[90:91] op_sel_hi:[0,1,1]
	v_lshlrev_b32_e32 v108, 16, v92
	v_and_b32_e32 v109, 0xffff0000, v92
	s_waitcnt vmcnt(11)
	v_lshlrev_b32_e32 v192, 16, v132
	v_and_b32_e32 v193, 0xffff0000, v132
	s_waitcnt vmcnt(7)
	v_lshlrev_b32_e32 v200, 16, v140
	v_and_b32_e32 v201, 0xffff0000, v140
	s_waitcnt vmcnt(3)
	v_lshlrev_b32_e32 v208, 16, v148
	v_and_b32_e32 v209, 0xffff0000, v148
	v_lshlrev_b32_e32 v158, 16, v110
	v_and_b32_e32 v159, 0xffff0000, v110
	v_pk_fma_f32 v[88:89], v[70:71], v[156:157], v[88:89] op_sel_hi:[0,1,1]
	v_lshlrev_b32_e32 v156, 16, v94
	v_and_b32_e32 v157, 0xffff0000, v94
	v_lshlrev_b32_e32 v92, 16, v93
	v_and_b32_e32 v93, 0xffff0000, v93
	v_and_b32_e32 v187, 0xffff0000, v126
	v_lshlrev_b32_e32 v124, 16, v125
	v_and_b32_e32 v125, 0xffff0000, v125
	v_lshlrev_b32_e32 v194, 16, v134
	v_and_b32_e32 v195, 0xffff0000, v134
	v_lshlrev_b32_e32 v132, 16, v133
	v_and_b32_e32 v133, 0xffff0000, v133
	v_lshlrev_b32_e32 v202, 16, v142
	v_and_b32_e32 v203, 0xffff0000, v142
	v_lshlrev_b32_e32 v140, 16, v141
	v_and_b32_e32 v141, 0xffff0000, v141
	s_waitcnt vmcnt(2)
	v_lshlrev_b32_e32 v210, 16, v150
	v_and_b32_e32 v211, 0xffff0000, v150
	v_lshlrev_b32_e32 v148, 16, v149
	v_and_b32_e32 v149, 0xffff0000, v149
	v_pk_fma_f32 v[58:59], v[70:71], v[108:109], v[58:59] op_sel_hi:[0,1,1]
	v_pk_fma_f32 v[50:51], v[70:71], v[184:185], v[50:51] op_sel_hi:[0,1,1]
	v_pk_fma_f32 v[42:43], v[70:71], v[192:193], v[42:43] op_sel_hi:[0,1,1]
	v_pk_fma_f32 v[38:39], v[70:71], v[200:201], v[38:39] op_sel_hi:[0,1,1]
	v_pk_fma_f32 v[34:35], v[70:71], v[208:209], v[34:35] op_sel_hi:[0,1,1]
	v_lshlrev_b32_e32 v160, 16, v112
	v_and_b32_e32 v161, 0xffff0000, v112
	v_lshlrev_b32_e32 v110, 16, v111
	v_and_b32_e32 v111, 0xffff0000, v111
	v_lshlrev_b32_e32 v94, 16, v95
	v_and_b32_e32 v95, 0xffff0000, v95
	v_lshlrev_b32_e32 v170, 16, v102
	v_and_b32_e32 v171, 0xffff0000, v102
	v_lshlrev_b32_e32 v102, 16, v103
	v_and_b32_e32 v103, 0xffff0000, v103
	v_lshlrev_b32_e32 v178, 16, v118
	v_and_b32_e32 v179, 0xffff0000, v118
	v_lshlrev_b32_e32 v118, 16, v119
	v_and_b32_e32 v119, 0xffff0000, v119
	v_lshlrev_b32_e32 v188, 16, v128
	v_and_b32_e32 v189, 0xffff0000, v128
	v_lshlrev_b32_e32 v126, 16, v127
	v_and_b32_e32 v127, 0xffff0000, v127
	v_lshlrev_b32_e32 v196, 16, v136
	v_and_b32_e32 v197, 0xffff0000, v136
	v_lshlrev_b32_e32 v134, 16, v135
	v_and_b32_e32 v135, 0xffff0000, v135
	v_lshlrev_b32_e32 v204, 16, v144
	v_and_b32_e32 v205, 0xffff0000, v144
	v_lshlrev_b32_e32 v142, 16, v143
	v_and_b32_e32 v143, 0xffff0000, v143
	s_waitcnt vmcnt(1)
; __device__ __forceinline__ void combine_row(int m, int lane, const float* __restrict__ h1, const bf16* __restrict__ y, const unsigned* __restrict__ cnt, const int* __restrict__ tok_e, const int* __restrict__ tok_p, ...
;     ...
;     for (int j = 0; j < 8; ++j) {
;         const int idx = j * 256 + lane * 4;
;         f32x4 a = *(const f32x4*)(h1 + (size_t)m * D + idx);
; #pragma unroll
;         for (int k = 0; k < 4; ++k) { const u32x2 w = *(const u32x2*)(y + yrow[k] + idx);
;             a.x += gk[k] * __uint_as_float(w.x << 16); a.y += gk[k] * __uint_as_float(w.x & 0xffff0000u); a.z += gk[k] * __uint_as_float(w.y << 16); a.w += gk[k] * __uint_as_float(w.y & 0xffff0000u); }
;         v[j] = a; ss += a.x * a.x + a.y * a.y + a.z * a.z + a.w * a.w;
	v_lshlrev_b32_e32 v212, 16, v152
	v_and_b32_e32 v213, 0xffff0000, v152
	v_lshlrev_b32_e32 v150, 16, v151
	v_and_b32_e32 v151, 0xffff0000, v151
	v_pk_fma_f32 v[88:89], v[68:69], v[158:159], v[88:89] op_sel_hi:[0,1,1]
	v_pk_fma_f32 v[60:61], v[70:71], v[92:93], v[60:61] op_sel_hi:[0,1,1]
	v_pk_fma_f32 v[54:55], v[70:71], v[168:169], v[54:55] op_sel_hi:[0,1,1]
	v_pk_fma_f32 v[56:57], v[70:71], v[100:101], v[56:57] op_sel_hi:[0,1,1]
	v_pk_fma_f32 v[46:47], v[70:71], v[176:177], v[46:47] op_sel_hi:[0,1,1]
	v_pk_fma_f32 v[48:49], v[70:71], v[116:117], v[48:49] op_sel_hi:[0,1,1]
	v_pk_fma_f32 v[52:53], v[70:71], v[124:125], v[52:53] op_sel_hi:[0,1,1]
	v_pk_fma_f32 v[44:45], v[70:71], v[132:133], v[44:45] op_sel_hi:[0,1,1]
	v_pk_fma_f32 v[40:41], v[70:71], v[140:141], v[40:41] op_sel_hi:[0,1,1]
	v_pk_fma_f32 v[36:37], v[70:71], v[148:149], v[36:37] op_sel_hi:[0,1,1]
	v_pk_fma_f32 v[58:59], v[68:69], v[156:157], v[58:59] op_sel_hi:[0,1,1]
	v_pk_fma_f32 v[50:51], v[68:69], v[186:187], v[50:51] op_sel_hi:[0,1,1]
	v_pk_fma_f32 v[42:43], v[68:69], v[194:195], v[42:43] op_sel_hi:[0,1,1]
	v_pk_fma_f32 v[38:39], v[68:69], v[202:203], v[38:39] op_sel_hi:[0,1,1]
	v_pk_fma_f32 v[34:35], v[68:69], v[210:211], v[34:35] op_sel_hi:[0,1,1]
	v_lshlrev_b32_e32 v162, 16, v114
	v_and_b32_e32 v163, 0xffff0000, v114
	v_lshlrev_b32_e32 v112, 16, v113
	v_and_b32_e32 v113, 0xffff0000, v113
	v_lshlrev_b32_e32 v166, 16, v98
	v_and_b32_e32 v167, 0xffff0000, v98
	v_lshlrev_b32_e32 v96, 16, v97
	v_and_b32_e32 v97, 0xffff0000, v97
	v_lshlrev_b32_e32 v172, 16, v104
	v_and_b32_e32 v173, 0xffff0000, v104
	v_lshlrev_b32_e32 v104, 16, v105
	v_and_b32_e32 v105, 0xffff0000, v105
	v_lshlrev_b32_e32 v180, 16, v120
	v_and_b32_e32 v181, 0xffff0000, v120
	v_lshlrev_b32_e32 v120, 16, v121
	v_and_b32_e32 v121, 0xffff0000, v121
	v_lshlrev_b32_e32 v190, 16, v130
	v_and_b32_e32 v191, 0xffff0000, v130
	v_lshlrev_b32_e32 v128, 16, v129
	v_and_b32_e32 v129, 0xffff0000, v129
	v_lshlrev_b32_e32 v198, 16, v138
	v_and_b32_e32 v199, 0xffff0000, v138
	v_lshlrev_b32_e32 v136, 16, v137
	v_and_b32_e32 v137, 0xffff0000, v137
	v_lshlrev_b32_e32 v206, 16, v146
	v_and_b32_e32 v207, 0xffff0000, v146
	v_lshlrev_b32_e32 v144, 16, v145
	v_and_b32_e32 v145, 0xffff0000, v145
	s_waitcnt vmcnt(0)
	v_lshlrev_b32_e32 v214, 16, v154
	v_and_b32_e32 v215, 0xffff0000, v154
	v_lshlrev_b32_e32 v152, 16, v153
	v_and_b32_e32 v153, 0xffff0000, v153
	v_pk_fma_f32 v[90:91], v[68:69], v[110:111], v[90:91] op_sel_hi:[0,1,1]
	v_pk_fma_f32 v[70:71], v[72:73], v[160:161], v[88:89] op_sel_hi:[0,1,1]
	v_pk_fma_f32 v[60:61], v[68:69], v[94:95], v[60:61] op_sel_hi:[0,1,1]
	v_pk_fma_f32 v[54:55], v[68:69], v[170:171], v[54:55] op_sel_hi:[0,1,1]
	v_pk_fma_f32 v[56:57], v[68:69], v[102:103], v[56:57] op_sel_hi:[0,1,1]
	v_pk_fma_f32 v[46:47], v[68:69], v[178:179], v[46:47] op_sel_hi:[0,1,1]
	v_pk_fma_f32 v[48:49], v[68:69], v[118:119], v[48:49] op_sel_hi:[0,1,1]
	v_pk_fma_f32 v[52:53], v[68:69], v[126:127], v[52:53] op_sel_hi:[0,1,1]
	v_pk_fma_f32 v[44:45], v[68:69], v[134:135], v[44:45] op_sel_hi:[0,1,1]
	v_pk_fma_f32 v[40:41], v[68:69], v[142:143], v[40:41] op_sel_hi:[0,1,1]
	v_pk_fma_f32 v[36:37], v[68:69], v[150:151], v[36:37] op_sel_hi:[0,1,1]
	v_pk_fma_f32 v[58:59], v[72:73], v[164:165], v[58:59] op_sel_hi:[0,1,1]
	v_pk_fma_f32 v[50:51], v[72:73], v[188:189], v[50:51] op_sel_hi:[0,1,1]
	v_pk_fma_f32 v[42:43], v[72:73], v[196:197], v[42:43] op_sel_hi:[0,1,1]
	v_pk_fma_f32 v[38:39], v[72:73], v[204:205], v[38:39] op_sel_hi:[0,1,1]
	v_pk_fma_f32 v[34:35], v[72:73], v[212:213], v[34:35] op_sel_hi:[0,1,1]
	v_lshlrev_b32_e32 v114, 16, v115
	v_and_b32_e32 v115, 0xffff0000, v115
	v_lshlrev_b32_e32 v98, 16, v99
	v_and_b32_e32 v99, 0xffff0000, v99
	v_lshlrev_b32_e32 v174, 16, v106
	v_and_b32_e32 v175, 0xffff0000, v106
	v_lshlrev_b32_e32 v106, 16, v107
	v_and_b32_e32 v107, 0xffff0000, v107
	v_lshlrev_b32_e32 v182, 16, v122
	v_and_b32_e32 v183, 0xffff0000, v122
	v_lshlrev_b32_e32 v122, 16, v123
	v_and_b32_e32 v123, 0xffff0000, v123
	v_lshlrev_b32_e32 v130, 16, v131
	v_and_b32_e32 v131, 0xffff0000, v131
	v_lshlrev_b32_e32 v138, 16, v139
	v_and_b32_e32 v139, 0xffff0000, v139
	v_lshlrev_b32_e32 v146, 16, v147
	v_and_b32_e32 v147, 0xffff0000, v147
	v_lshlrev_b32_e32 v154, 16, v155
	v_and_b32_e32 v155, 0xffff0000, v155
	v_pk_fma_f32 v[88:89], v[72:73], v[112:113], v[90:91] op_sel_hi:[0,1,1]
	v_pk_fma_f32 v[68:69], v[72:73], v[162:163], v[70:71] op_sel:[1,0,0]
	v_pk_fma_f32 v[60:61], v[72:73], v[96:97], v[60:61] op_sel_hi:[0,1,1]
	v_pk_fma_f32 v[54:55], v[72:73], v[172:173], v[54:55] op_sel_hi:[0,1,1]
	v_pk_fma_f32 v[56:57], v[72:73], v[104:105], v[56:57] op_sel_hi:[0,1,1]
	v_pk_fma_f32 v[46:47], v[72:73], v[180:181], v[46:47] op_sel_hi:[0,1,1]
	v_pk_fma_f32 v[48:49], v[72:73], v[120:121], v[48:49] op_sel_hi:[0,1,1]
	v_pk_fma_f32 v[52:53], v[72:73], v[128:129], v[52:53] op_sel_hi:[0,1,1]
	v_pk_fma_f32 v[44:45], v[72:73], v[136:137], v[44:45] op_sel_hi:[0,1,1]
	v_pk_fma_f32 v[40:41], v[72:73], v[144:145], v[40:41] op_sel_hi:[0,1,1]
	v_pk_fma_f32 v[36:37], v[72:73], v[152:153], v[36:37] op_sel_hi:[0,1,1]
	v_pk_fma_f32 v[58:59], v[72:73], v[166:167], v[58:59] op_sel:[1,0,0]
	v_pk_fma_f32 v[50:51], v[72:73], v[190:191], v[50:51] op_sel:[1,0,0]
	v_pk_fma_f32 v[42:43], v[72:73], v[198:199], v[42:43] op_sel:[1,0,0]
	v_pk_fma_f32 v[38:39], v[72:73], v[206:207], v[38:39] op_sel:[1,0,0]
; __device__ __forceinline__ float wave_sum(float v) {
; #pragma unroll
;     for (int o = 1; o < 64; o <<= 1) v += __shfl_xor(v, o);
;     return v;
; }
; __device__ __forceinline__ void combine_row(int m, int lane, const float* __restrict__ h1, const bf16* __restrict__ y, const unsigned* __restrict__ cnt, const int* __restrict__ tok_e, const int* __restrict__ tok_p, ...
;     ...
;         v[j] = a; ss += a.x * a.x + a.y * a.y + a.z * a.z + a.w * a.w;
;     }
;     const float rstd = rsqrtf(wave_sum(ss) * (1.f / D) + EPS);
; #pragma unroll
;     for (int j = 0; j < 8; ++j) { const int idx = j * 256 + lane * 4; const f32x4 gg = *(const f32x4*)(g_final + idx);
;         *(f32x4*)(out + (size_t)m * D + idx) = (f32x4){v[j].x * rstd * gg.x, v[j].y * rstd * gg.y, v[j].z * rstd * gg.z, v[j].w * rstd * gg.w}; }
	v_pk_fma_f32 v[34:35], v[72:73], v[214:215], v[34:35] op_sel:[1,0,0]
	v_pk_fma_f32 v[70:71], v[72:73], v[114:115], v[88:89] op_sel:[1,0,0]
	v_pk_mul_f32 v[88:89], v[68:69], v[68:69]
	v_pk_fma_f32 v[60:61], v[72:73], v[98:99], v[60:61] op_sel:[1,0,0]
	v_pk_fma_f32 v[54:55], v[72:73], v[174:175], v[54:55] op_sel:[1,0,0]
	v_pk_fma_f32 v[56:57], v[72:73], v[106:107], v[56:57] op_sel:[1,0,0]
	v_pk_fma_f32 v[46:47], v[72:73], v[182:183], v[46:47] op_sel:[1,0,0]
	v_pk_fma_f32 v[48:49], v[72:73], v[122:123], v[48:49] op_sel:[1,0,0]
	v_pk_fma_f32 v[52:53], v[72:73], v[130:131], v[52:53] op_sel:[1,0,0]
	v_pk_fma_f32 v[44:45], v[72:73], v[138:139], v[44:45] op_sel:[1,0,0]
	v_pk_fma_f32 v[40:41], v[72:73], v[146:147], v[40:41] op_sel:[1,0,0]
	v_pk_fma_f32 v[36:37], v[72:73], v[154:155], v[36:37] op_sel:[1,0,0]
	v_pk_mul_f32 v[72:73], v[58:59], v[58:59]
	v_mov_b32_e32 v104, v51
	v_mov_b32_e32 v105, v43
	v_mov_b32_e32 v112, v39
	v_mov_b32_e32 v113, v35
	v_pk_mul_f32 v[90:91], v[70:71], v[70:71]
	v_pk_mul_f32 v[92:93], v[60:61], v[60:61]
	v_pk_mul_f32 v[94:95], v[54:55], v[54:55]
	v_add_f32_e32 v118, v88, v89
	v_pk_mul_f32 v[88:89], v[104:105], v[104:105]
	v_pk_mul_f32 v[104:105], v[112:113], v[112:113]
	v_add_f32_e32 v112, v72, v73
	v_pk_mul_f32 v[96:97], v[56:57], v[56:57]
	v_pk_mul_f32 v[98:99], v[46:47], v[46:47]
	v_add_f32_e32 v90, v90, v118
	v_add_f32_e32 v94, v94, v95
	v_add_f32_e32 v92, v92, v112
	v_pk_mul_f32 v[100:101], v[48:49], v[48:49]
	v_mov_b32_e32 v102, v50
	v_mov_b32_e32 v103, v42
	v_add_f32_e32 v95, v98, v99
	v_add_f32_e32 v90, v91, v90
	v_add_f32_e32 v91, v96, v94
	v_add_f32_e32 v92, v93, v92
	v_mov_b32_e32 v106, v52
	v_mov_b32_e32 v107, v44
	v_pk_fma_f32 v[72:73], v[102:103], v[102:103], v[88:89]
	v_add_f32_e32 v94, v100, v95
	v_add_f32_e32 v91, v97, v91
	v_add_f32_e32 v90, v90, v92
	v_mov_b32_e32 v108, v53
	v_mov_b32_e32 v109, v45
	v_mov_b32_e32 v110, v38
	v_mov_b32_e32 v111, v34
	v_pk_fma_f32 v[72:73], v[106:107], v[106:107], v[72:73]
	v_add_f32_e32 v93, v101, v94
	v_add_f32_e32 v90, v90, v91
	v_mov_b32_e32 v114, v40
	v_mov_b32_e32 v115, v36
	v_pk_fma_f32 v[88:89], v[110:111], v[110:111], v[104:105]
	v_pk_fma_f32 v[72:73], v[108:109], v[108:109], v[72:73]
	v_add_f32_e32 v90, v90, v93
	v_mov_b32_e32 v116, v41
	v_mov_b32_e32 v117, v37
	v_pk_fma_f32 v[88:89], v[114:115], v[114:115], v[88:89]
	v_add_f32_e32 v72, v90, v72
	v_pk_fma_f32 v[88:89], v[116:117], v[116:117], v[88:89]
	v_add_f32_e32 v72, v72, v73
	v_add_f32_e32 v72, v72, v88
	v_add_f32_e32 v72, v72, v89
	ds_bpermute_b32 v73, v74, v72
	s_waitcnt lgkmcnt(0)
	v_add_f32_e32 v72, v72, v73
	ds_bpermute_b32 v73, v75, v72
	s_waitcnt lgkmcnt(0)
	v_add_f32_e32 v72, v72, v73
	ds_bpermute_b32 v73, v76, v72
	s_waitcnt lgkmcnt(0)
	v_add_f32_e32 v72, v72, v73
	ds_bpermute_b32 v73, v77, v72
	s_waitcnt lgkmcnt(0)
	v_add_f32_e32 v72, v72, v73
	ds_bpermute_b32 v73, v78, v72
	s_waitcnt lgkmcnt(0)
	v_add_f32_e32 v72, v72, v73
	ds_bpermute_b32 v73, v79, v72
	s_waitcnt lgkmcnt(0)
	v_add_f32_e32 v72, v72, v73
	v_fmamk_f32 v72, v72, 0x3a000000, v87
	v_mul_f32_e32 v73, 0x4b800000, v72
	v_cmp_gt_f32_e32 vcc, s25, v72
	s_nop 1
	v_cndmask_b32_e32 v72, v72, v73, vcc
	v_rsq_f32_e32 v72, v72
	s_nop 0
	v_mul_f32_e32 v73, 0x45800000, v72
	v_cndmask_b32_e32 v72, v72, v73, vcc
	v_pk_mul_f32 v[68:69], v[68:69], v[72:73] op_sel_hi:[1,0]
	v_pk_mul_f32 v[70:71], v[70:71], v[72:73] op_sel_hi:[1,0]
	v_pk_mul_f32 v[58:59], v[58:59], v[72:73] op_sel_hi:[1,0]
	v_pk_mul_f32 v[60:61], v[60:61], v[72:73] op_sel_hi:[1,0]
	v_pk_mul_f32 v[54:55], v[54:55], v[72:73] op_sel_hi:[1,0]
	v_pk_mul_f32 v[56:57], v[56:57], v[72:73] op_sel_hi:[1,0]
	v_pk_mul_f32 v[46:47], v[46:47], v[72:73] op_sel_hi:[1,0]
	v_pk_mul_f32 v[48:49], v[48:49], v[72:73] op_sel_hi:[1,0]
	v_pk_mul_f32 v[50:51], v[50:51], v[72:73] op_sel_hi:[1,0]
	v_pk_mul_f32 v[52:53], v[52:53], v[72:73] op_sel_hi:[1,0]
	v_pk_mul_f32 v[88:89], v[42:43], v[72:73] op_sel_hi:[1,0]
	v_pk_mul_f32 v[90:91], v[44:45], v[72:73] op_sel_hi:[1,0]
	v_pk_mul_f32 v[92:93], v[38:39], v[72:73] op_sel_hi:[1,0]
	v_pk_mul_f32 v[94:95], v[40:41], v[72:73] op_sel_hi:[1,0]
	v_pk_mul_f32 v[96:97], v[34:35], v[72:73] op_sel_hi:[1,0]
	v_pk_mul_f32 v[72:73], v[36:37], v[72:73] op_sel_hi:[1,0]
	v_pk_mul_f32 v[36:37], v[4:5], v[70:71]
	v_pk_mul_f32 v[34:35], v[2:3], v[68:69]
	v_pk_mul_f32 v[40:41], v[8:9], v[60:61]
	v_pk_mul_f32 v[38:39], v[6:7], v[58:59]
	v_pk_mul_f32 v[44:45], v[12:13], v[56:57]
	v_pk_mul_f32 v[42:43], v[10:11], v[54:55]
	v_pk_mul_f32 v[48:49], v[16:17], v[48:49]
	v_pk_mul_f32 v[46:47], v[14:15], v[46:47]
	v_pk_mul_f32 v[52:53], v[20:21], v[52:53]
	v_pk_mul_f32 v[50:51], v[18:19], v[50:51]
	v_pk_mul_f32 v[56:57], v[24:25], v[90:91]
	v_pk_mul_f32 v[54:55], v[22:23], v[88:89]
	v_pk_mul_f32 v[60:61], v[28:29], v[94:95]
	v_pk_mul_f32 v[58:59], v[26:27], v[92:93]
	v_pk_mul_f32 v[70:71], v[32:33], v[72:73]
	v_pk_mul_f32 v[68:69], v[30:31], v[96:97]
	global_store_dwordx4 v[0:1], v[34:37], off
	global_store_dwordx4 v[0:1], v[38:41], off offset:1024
	global_store_dwordx4 v[0:1], v[42:45], off offset:2048
	global_store_dwordx4 v[0:1], v[46:49], off offset:3072
	global_store_dwordx4 v[66:67], v[50:53], off
	global_store_dwordx4 v[66:67], v[54:57], off offset:1024
	global_store_dwordx4 v[66:67], v[58:61], off offset:2048
	global_store_dwordx4 v[66:67], v[68:71], off offset:3072
	s_cbranch_scc1 .LBB0_1579

; __global__ void __launch_bounds__(NWAVES * 64, 2) mk_fwd(Args a) {
	.amdhsa_kernel _Z6mk_fwd4Args
		.amdhsa_group_segment_fixed_size 0
		.amdhsa_private_segment_fixed_size 0
		.amdhsa_kernarg_size 440
		.amdhsa_user_sgpr_count 2
		.amdhsa_user_sgpr_dispatch_ptr 0
		.amdhsa_user_sgpr_queue_ptr 0
		.amdhsa_user_sgpr_kernarg_segment_ptr 1
		.amdhsa_user_sgpr_dispatch_id 0
		.amdhsa_user_sgpr_kernarg_preload_length 0
		.amdhsa_user_sgpr_kernarg_preload_offset 0
		.amdhsa_user_sgpr_private_segment_size 0
		.amdhsa_uses_dynamic_stack 0
		.amdhsa_enable_private_segment 0
		.amdhsa_system_sgpr_workgroup_id_x 1
		.amdhsa_system_sgpr_workgroup_id_y 0
		.amdhsa_system_sgpr_workgroup_id_z 0
		.amdhsa_system_sgpr_workgroup_info 0
		.amdhsa_system_vgpr_workitem_id 0
		.amdhsa_next_free_vgpr 253
		.amdhsa_next_free_sgpr 100
		.amdhsa_accum_offset 256
		.amdhsa_reserve_vcc 1
		.amdhsa_float_round_mode_32 0
		.amdhsa_float_round_mode_16_64 0
		.amdhsa_float_denorm_mode_32 3
		.amdhsa_float_denorm_mode_16_64 3
		.amdhsa_dx10_clamp 1
		.amdhsa_ieee_mode 1
		.amdhsa_fp16_overflow 0
		.amdhsa_tg_split 0
		.amdhsa_exception_fp_ieee_invalid_op 0
		.amdhsa_exception_fp_denorm_src 0
		.amdhsa_exception_fp_ieee_div_zero 0
		.amdhsa_exception_fp_ieee_overflow 0
		.amdhsa_exception_fp_ieee_underflow 0
		.amdhsa_exception_fp_ieee_inexact 0
		.amdhsa_exception_int_div_zero 0
	.end_amdhsa_kernel

; __global__ void __launch_bounds__(NWAVES * 64, 2) mk_fwd(Args a) {
amdhsa.kernels:
  - .agpr_count:     0
    .args:
      - .offset:         0
        .size:           184
        .value_kind:     by_value
      - .offset:         184
        .size:           4
        .value_kind:     hidden_block_count_x
      - .offset:         188
        .size:           4
        .value_kind:     hidden_block_count_y
      - .offset:         192
        .size:           4
        .value_kind:     hidden_block_count_z
      - .offset:         196
        .size:           2
        .value_kind:     hidden_group_size_x
      - .offset:         198
        .size:           2
        .value_kind:     hidden_group_size_y
      - .offset:         200
        .size:           2
        .value_kind:     hidden_group_size_z
      - .offset:         202
        .size:           2
        .value_kind:     hidden_remainder_x
      - .offset:         204
        .size:           2
        .value_kind:     hidden_remainder_y
      - .offset:         206
        .size:           2
        .value_kind:     hidden_remainder_z
      - .offset:         224
        .size:           8
        .value_kind:     hidden_global_offset_x
      - .offset:         232
        .size:           8
        .value_kind:     hidden_global_offset_y
      - .offset:         240
        .size:           8
        .value_kind:     hidden_global_offset_z
      - .offset:         248
        .size:           2
        .value_kind:     hidden_grid_dims
      - .offset:         304
        .size:           4
        .value_kind:     hidden_dynamic_lds_size
    .group_segment_fixed_size: 0
    .kernarg_segment_align: 8
    .kernarg_segment_size: 440
    .language:       OpenCL C
    .language_version:
      - 2
      - 0
    .max_flat_workgroup_size: 512
    .name:           _Z6mk_fwd4Args
    .private_segment_fixed_size: 0
    .sgpr_count:     106
    .sgpr_spill_count: 21
    .symbol:         _Z6mk_fwd4Args.kd
    .uniform_work_group_size: 1
    .uses_dynamic_stack: false
    .vgpr_count:     253
    .vgpr_spill_count: 0
    .wavefront_size: 64
